# stack on v45: attention back-edge rotation + MoE gather via 32-bit saddr offsets (no LDS index reads or drains in loop) + S5 part-2 diagonal sd load hoisted to loop top
# speedup vs baseline: 1.0008x; 1.0008x over previous
.LBB0_292:
	s_mov_b32 s64, 0x2aaaaaab
	s_waitcnt vmcnt(0)
	v_mul_hi_i32 v4, v46, s64
	v_lshrrev_b32_e32 v5, 31, v4
	v_ashrrev_i32_e32 v4, 3, v4
	v_add_u32_e32 v55, v4, v5
	s_movk_i32 s74, 0xffd0
	v_mad_u64_u32 v[48:49], s[74:75], v55, s74, v[46:47]
	v_ashrrev_i32_e32 v51, 4, v55
	v_and_b32_e32 v50, 15, v55
	v_lshlrev_b32_e32 v253, 2, v50
	global_load_dword v252, v253, s[88:89]
	v_cmp_lt_i32_e64 s[74:75], 31, v48
	s_and_saveexec_b64 s[76:77], s[74:75]
	s_xor_b64 s[76:77], exec, s[76:77]
	s_cbranch_execz .LBB0_294
	v_lshlrev_b32_e32 v4, 2, v54
	v_and_b32_e32 v4, 0xe0, v4
	v_lshl_or_b32 v5, v50, 8, v4
	v_lshl_or_b32 v4, v51, 8, v4
	v_add_u32_e32 v49, 0, v5
	v_add_u32_e32 v72, 0, v4
	ds_read_b128 v[4:7], v49 offset:25088
	ds_read_b128 v[8:11], v49 offset:25104
	ds_read_b128 v[50:53], v49 offset:29184
	ds_read_b128 v[56:59], v72 offset:20992
	ds_read_b128 v[60:63], v72 offset:16640
	ds_read_b128 v[64:67], v72 offset:16656
	ds_read_b128 v[68:71], v49 offset:29200
	ds_read_b128 v[72:75], v72 offset:21008
	s_waitcnt lgkmcnt(4)
	v_pk_mul_f32 v[76:77], v[50:51], v[56:57]
	v_pk_mul_f32 v[56:57], v[4:5], v[56:57]
	s_waitcnt lgkmcnt(2)
	v_mul_f32_e32 v82, v10, v66
	s_waitcnt lgkmcnt(1)
	v_mul_f32_e32 v66, v70, v66
	s_waitcnt lgkmcnt(0)
	v_mul_f32_e32 v84, v70, v74
	v_mul_f32_e32 v86, v10, v74
	v_mov_b32_e32 v70, v11
	v_mov_b32_e32 v74, v67
	v_mov_b32_e32 v10, v71
	v_pk_mul_f32 v[88:89], v[70:71], v[74:75]
	v_pk_mul_f32 v[10:11], v[10:11], v[74:75]
	v_pk_mul_f32 v[78:79], v[52:53], v[58:59]
	v_pk_mul_f32 v[58:59], v[6:7], v[58:59]
	v_pk_mul_f32 v[80:81], v[68:69], v[72:73]
	v_pk_mul_f32 v[72:73], v[8:9], v[72:73]
	v_mov_b32_e32 v83, v88
	v_mov_b32_e32 v85, v89
	v_mov_b32_e32 v67, v10
	v_mov_b32_e32 v87, v11
	v_pk_fma_f32 v[4:5], v[4:5], v[60:61], v[76:77] neg_lo:[0,0,1] neg_hi:[0,0,1]
	v_pk_fma_f32 v[6:7], v[6:7], v[62:63], v[78:79] neg_lo:[0,0,1] neg_hi:[0,0,1]
	v_pk_fma_f32 v[8:9], v[8:9], v[64:65], v[80:81] neg_lo:[0,0,1] neg_hi:[0,0,1]
	v_pk_add_f32 v[10:11], v[82:83], v[84:85] neg_lo:[0,1] neg_hi:[0,1]
	v_pk_fma_f32 v[50:51], v[50:51], v[60:61], v[56:57]
	v_pk_fma_f32 v[52:53], v[52:53], v[62:63], v[58:59]
	v_pk_fma_f32 v[56:57], v[68:69], v[64:65], v[72:73]
	v_pk_add_f32 v[58:59], v[66:67], v[86:87]
	v_cmp_gt_u32_e64 s[74:75], 40, v48
	s_nop 1
	v_cndmask_b32_e64 v11, -v59, v11, s[74:75]
	v_cndmask_b32_e64 v10, -v58, v10, s[74:75]
	v_cndmask_b32_e64 v7, -v53, v7, s[74:75]
	v_cndmask_b32_e64 v6, -v52, v6, s[74:75]
	v_cndmask_b32_e64 v9, -v57, v9, s[74:75]
	v_cndmask_b32_e64 v8, -v56, v8, s[74:75]
	v_cndmask_b32_e64 v5, -v51, v5, s[74:75]
	v_cndmask_b32_e64 v4, -v50, v4, s[74:75]
.LBB0_294:
	s_andn2_saveexec_b64 s[90:91], s[76:77]
	s_cbranch_execz .LBB0_291
	v_ashrrev_i32_e32 v5, 1, v48
	v_and_b32_e32 v49, 8, v54
	v_sub_u32_e32 v4, v51, v5
	v_lshl_add_u32 v4, v4, 10, 0
	v_lshlrev_b32_e32 v6, 6, v50
	v_lshlrev_b32_e32 v7, 2, v49
	v_cmp_ge_i32_e64 s[74:75], v51, v5
	v_add3_u32 v56, v4, v6, v7
	v_mov_b32_e32 v4, 0
	s_and_saveexec_b64 s[76:77], s[74:75]
	ds_read_b32 v4, v56
	s_or_b64 exec, exec, s[76:77]
	v_cmp_eq_u32_e64 s[76:77], v51, v5
	v_mov_b32_e32 v51, v2
	v_cmp_eq_u32_e64 s[78:79], v50, v49
	v_lshl_add_u64 v[52:53], v[50:51], 2, s[88:89]
	s_and_b64 s[96:97], s[76:77], s[78:79]
	s_and_saveexec_b64 s[78:79], s[96:97]
	s_cbranch_execz .LBB0_299
	s_waitcnt vmcnt(0) lgkmcnt(0)
	v_mov_b32_e32 v5, v252
	v_add_f32_e32 v4, v4, v5
.LBB0_299:
	s_or_b64 exec, exec, s[78:79]
	v_mov_b32_e32 v5, 0
	s_and_saveexec_b64 s[78:79], s[74:75]
	ds_read_b32 v5, v56 offset:4
	s_or_b64 exec, exec, s[78:79]
	v_or_b32_e32 v6, 1, v49
	v_cmp_eq_u32_e64 s[78:79], v50, v6
	s_and_b64 s[96:97], s[76:77], s[78:79]
	s_and_saveexec_b64 s[78:79], s[96:97]
	s_cbranch_execz .LBB0_303
	s_waitcnt vmcnt(0) lgkmcnt(0)
	v_mov_b32_e32 v6, v252
	v_add_f32_e32 v5, v5, v6
.LBB0_303:
	s_or_b64 exec, exec, s[78:79]
	v_mov_b32_e32 v6, 0
	s_and_saveexec_b64 s[78:79], s[74:75]
	ds_read_b32 v6, v56 offset:8
	s_or_b64 exec, exec, s[78:79]
	v_or_b32_e32 v7, 2, v49
	v_cmp_eq_u32_e64 s[78:79], v50, v7
	s_and_b64 s[96:97], s[76:77], s[78:79]
	s_and_saveexec_b64 s[78:79], s[96:97]
	s_cbranch_execz .LBB0_307
	s_waitcnt vmcnt(0) lgkmcnt(0)
	v_mov_b32_e32 v7, v252
	v_add_f32_e32 v6, v6, v7
.LBB0_307:
	s_or_b64 exec, exec, s[78:79]
	v_mov_b32_e32 v7, 0
	s_and_saveexec_b64 s[78:79], s[74:75]
	ds_read_b32 v7, v56 offset:12
	s_or_b64 exec, exec, s[78:79]
	v_or_b32_e32 v8, 3, v49
	v_cmp_eq_u32_e64 s[78:79], v50, v8
	s_and_b64 s[96:97], s[76:77], s[78:79]
	s_and_saveexec_b64 s[78:79], s[96:97]
	s_cbranch_execz .LBB0_311
	s_waitcnt vmcnt(0) lgkmcnt(0)
	v_mov_b32_e32 v8, v252
	v_add_f32_e32 v7, v7, v8
.LBB0_311:
	s_or_b64 exec, exec, s[78:79]
	v_mov_b32_e32 v8, 0
	s_and_saveexec_b64 s[78:79], s[74:75]
	ds_read_b32 v8, v56 offset:16
	s_or_b64 exec, exec, s[78:79]
	v_or_b32_e32 v9, 4, v49
	v_cmp_eq_u32_e64 s[78:79], v50, v9
	s_and_b64 s[96:97], s[76:77], s[78:79]
	s_and_saveexec_b64 s[78:79], s[96:97]
	s_cbranch_execz .LBB0_315
	s_waitcnt vmcnt(0) lgkmcnt(0)
	v_mov_b32_e32 v9, v252
	v_add_f32_e32 v8, v8, v9
.LBB0_315:
	s_or_b64 exec, exec, s[78:79]
	v_mov_b32_e32 v9, 0
	s_and_saveexec_b64 s[78:79], s[74:75]
	ds_read_b32 v9, v56 offset:20
	s_or_b64 exec, exec, s[78:79]
	v_or_b32_e32 v10, 5, v49
	v_cmp_eq_u32_e64 s[78:79], v50, v10
	s_and_b64 s[96:97], s[76:77], s[78:79]
	s_and_saveexec_b64 s[78:79], s[96:97]
	s_cbranch_execz .LBB0_319
	s_waitcnt vmcnt(0) lgkmcnt(0)
	v_mov_b32_e32 v10, v252
	v_add_f32_e32 v9, v9, v10
.LBB0_319:
	s_or_b64 exec, exec, s[78:79]
	v_mov_b32_e32 v10, 0
	s_and_saveexec_b64 s[78:79], s[74:75]
	ds_read_b32 v10, v56 offset:24
	s_or_b64 exec, exec, s[78:79]
	v_or_b32_e32 v11, 6, v49
	v_cmp_eq_u32_e64 s[78:79], v50, v11
	s_and_b64 s[96:97], s[76:77], s[78:79]
	s_and_saveexec_b64 s[78:79], s[96:97]
	s_cbranch_execz .LBB0_323
	s_waitcnt vmcnt(0) lgkmcnt(0)
	v_mov_b32_e32 v11, v252
	v_add_f32_e32 v10, v10, v11
.LBB0_323:
	s_or_b64 exec, exec, s[78:79]
	v_mov_b32_e32 v11, 0
	s_and_saveexec_b64 s[78:79], s[74:75]
	ds_read_b32 v11, v56 offset:28
	s_or_b64 exec, exec, s[78:79]
	v_or_b32_e32 v49, 7, v49
	v_cmp_eq_u32_e64 s[74:75], v50, v49
	s_and_b64 s[76:77], s[76:77], s[74:75]
	s_and_saveexec_b64 s[74:75], s[76:77]
	s_cbranch_execz .LBB0_290
	s_waitcnt vmcnt(0) lgkmcnt(0)
	v_mov_b32_e32 v49, v252
	v_add_f32_e32 v11, v11, v49
	s_branch .LBB0_290

.LBB0_1256:
	s_or_b64 exec, exec, s[38:39]
	v_mov_b32_e32 v34, v0
	s_waitcnt lgkmcnt(0)
	s_barrier
	s_movk_i32 s18, 0x100
	v_ashrrev_i32_e32 v35, 4, v34
	v_lshl_add_u32 v4, v35, 2, 0
	v_add_u32_e32 v233, 0x24d80, v4
	ds_read2_b32 v[6:7], v233 offset1:32
	v_lshlrev_b32_e32 v4, 3, v34
	v_and_b32_e32 v234, 0x78, v4
	v_readfirstlane_b32 s12, v34
	v_cmp_gt_i32_e64 s[48:49], s18, v34
	s_waitcnt lgkmcnt(0)
	v_lshlrev_b32_e32 v252, 11, v6
	v_lshlrev_b32_e32 v253, 11, v7
	v_ashrrev_i32_e32 v5, 31, v6
	v_mov_b32_e32 v4, v6
	v_lshlrev_b64 v[4:5], 11, v[4:5]
	v_lshl_add_u64 v[8:9], s[6:7], 0, v[4:5]
	v_lshlrev_b32_e32 v4, 1, v234
	v_mov_b32_e32 v5, v2
	v_lshl_add_u64 v[10:11], v[8:9], 0, v[4:5]
	v_ashrrev_i32_e32 v9, 31, v7
	v_mov_b32_e32 v8, v7
	v_lshlrev_b64 v[6:7], 11, v[8:9]
	ds_read2_b32 v[8:9], v233 offset0:64 offset1:96
	v_lshl_add_u64 v[6:7], s[6:7], 0, v[6:7]
	v_lshl_add_u64 v[12:13], v[6:7], 0, v[4:5]
	global_load_dwordx4 v[14:17], v[10:11], off
	global_load_dwordx4 v[18:21], v[12:13], off
	s_waitcnt lgkmcnt(0)
	v_lshlrev_b32_e32 v254, 11, v8
	v_lshlrev_b32_e32 v255, 11, v9
	v_ashrrev_i32_e32 v7, 31, v8
	v_mov_b32_e32 v6, v8
	v_lshlrev_b64 v[6:7], 11, v[6:7]
	v_lshl_add_u64 v[6:7], s[6:7], 0, v[6:7]
	v_lshl_add_u64 v[30:31], v[6:7], 0, v[4:5]
	v_ashrrev_i32_e32 v7, 31, v9
	v_mov_b32_e32 v6, v9
	v_lshlrev_b64 v[6:7], 11, v[6:7]
	v_lshl_add_u64 v[6:7], s[6:7], 0, v[6:7]
	v_lshl_add_u64 v[32:33], v[6:7], 0, v[4:5]
	global_load_dwordx4 v[22:25], v[30:31], off
	global_load_dwordx4 v[26:29], v[32:33], off
	s_and_saveexec_b64 s[38:39], s[48:49]
	s_cbranch_execz .LBB0_1258
	ds_read_b32 v6, v233 offset:512
	s_waitcnt lgkmcnt(0)
	v_ashrrev_i32_e32 v7, 31, v6
	v_lshlrev_b64 v[6:7], 11, v[6:7]
	v_lshl_add_u64 v[6:7], s[6:7], 0, v[6:7]
	v_lshl_add_u64 v[6:7], v[6:7], 0, v[4:5]
	global_load_dwordx4 v[6:9], v[6:7], off

.LBB0_1266:
	v_lshl_or_b32 v4, s67, 7, v234
	v_ashrrev_i32_e32 v5, 31, v4
	v_lshlrev_b32_e32 v122, 1, v4
	v_add_u32_e32 v124, v252, v122
	v_add_u32_e32 v126, v253, v122
	global_load_dwordx4 v[142:145], v124, s[6:7]
	s_nop 0
	global_load_dwordx4 v[126:129], v126, s[6:7]
	s_waitcnt vmcnt(9) lgkmcnt(3)
	v_mfma_f32_16x16x32_bf16 v[182:185], v[166:169], v[198:201], v[182:185]
	s_waitcnt vmcnt(5)
	v_mfma_f32_16x16x32_bf16 v[162:165], v[174:177], v[198:201], v[162:165]
	v_mfma_f32_16x16x32_bf16 v[134:137], v[166:169], v[194:197], v[134:137]
	v_mfma_f32_16x16x32_bf16 v[118:121], v[174:177], v[194:197], v[118:121]
	v_mfma_f32_16x16x32_bf16 v[102:105], v[166:169], v[202:205], v[102:105]
	v_mfma_f32_16x16x32_bf16 v[86:89], v[174:177], v[202:205], v[86:89]

.LBB0_1270:
	v_add_u32_e32 v124, v254, v122
	v_add_u32_e32 v122, v255, v122
	global_load_dwordx4 v[130:133], v124, s[6:7]
	s_nop 0
	global_load_dwordx4 v[122:125], v122, s[6:7]
	s_waitcnt vmcnt(11) lgkmcnt(3)
	v_mfma_f32_16x16x32_bf16 v[82:85], v[166:169], v[18:21], v[82:85]
	s_waitcnt vmcnt(7)
	v_mfma_f32_16x16x32_bf16 v[78:81], v[174:177], v[18:21], v[78:81]
	v_mfma_f32_16x16x32_bf16 v[74:77], v[166:169], v[22:25], v[74:77]
	v_mfma_f32_16x16x32_bf16 v[70:73], v[174:177], v[22:25], v[70:73]
	v_mfma_f32_16x16x32_bf16 v[66:69], v[166:169], v[34:37], v[66:69]
	v_mfma_f32_16x16x32_bf16 v[62:65], v[174:177], v[34:37], v[62:65]

.LBB0_1276:
	s_or_b64 exec, exec, s[38:39]
	s_waitcnt vmcnt(11) lgkmcnt(3)
	v_mfma_f32_16x16x32_bf16 v[58:61], v[166:169], v[198:201], v[58:61]
	s_waitcnt vmcnt(7)
	v_mfma_f32_16x16x32_bf16 v[54:57], v[174:177], v[198:201], v[54:57]
	v_mfma_f32_16x16x32_bf16 v[50:53], v[166:169], v[194:197], v[50:53]
	v_mfma_f32_16x16x32_bf16 v[46:49], v[174:177], v[194:197], v[46:49]
	v_mfma_f32_16x16x32_bf16 v[42:45], v[166:169], v[202:205], v[42:45]
	v_mfma_f32_16x16x32_bf16 v[14:17], v[174:177], v[202:205], v[14:17]

.LBB0_1318:
	s_add_i32 s12, s67, 1
	s_cmp_lg_u32 s12, 8
	s_cselect_b32 s67, s12, 0
	v_lshl_or_b32 v4, s67, 7, v234
	v_ashrrev_i32_e32 v5, 31, v4
	v_lshlrev_b32_e32 v90, 1, v4
	v_add_u32_e32 v92, v252, v90
	v_add_u32_e32 v94, v253, v90
	global_load_dwordx4 v[106:109], v92, s[6:7]
	s_nop 0
	global_load_dwordx4 v[94:97], v94, s[6:7]
	s_waitcnt vmcnt(9) lgkmcnt(3)
	v_mfma_f32_16x16x32_bf16 v[182:185], v[166:169], v[198:201], v[182:185]
	s_waitcnt vmcnt(8)
	v_mfma_f32_16x16x32_bf16 v[162:165], v[174:177], v[198:201], v[162:165]
	v_mfma_f32_16x16x32_bf16 v[134:137], v[166:169], v[194:197], v[134:137]
	v_mfma_f32_16x16x32_bf16 v[118:121], v[174:177], v[194:197], v[118:121]
	v_mfma_f32_16x16x32_bf16 v[102:105], v[166:169], v[202:205], v[102:105]
	v_mfma_f32_16x16x32_bf16 v[86:89], v[174:177], v[202:205], v[86:89]

.LBB0_1322:
	v_add_u32_e32 v92, v254, v90
	v_add_u32_e32 v90, v255, v90
	global_load_dwordx4 v[98:101], v92, s[6:7]
	s_nop 0
	global_load_dwordx4 v[90:93], v90, s[6:7]
	s_waitcnt vmcnt(11) lgkmcnt(3)
	v_mfma_f32_16x16x32_bf16 v[82:85], v[166:169], v[26:29], v[82:85]
	s_waitcnt vmcnt(10)
	v_mfma_f32_16x16x32_bf16 v[78:81], v[174:177], v[26:29], v[78:81]
	v_mfma_f32_16x16x32_bf16 v[74:77], v[166:169], v[30:33], v[74:77]
	v_mfma_f32_16x16x32_bf16 v[70:73], v[174:177], v[30:33], v[70:73]
	v_mfma_f32_16x16x32_bf16 v[66:69], v[166:169], v[38:41], v[66:69]
	v_mfma_f32_16x16x32_bf16 v[62:65], v[174:177], v[38:41], v[62:65]

.LBB0_1328:
	s_or_b64 exec, exec, s[38:39]
	s_waitcnt vmcnt(11) lgkmcnt(3)
	v_mfma_f32_16x16x32_bf16 v[58:61], v[166:169], v[198:201], v[58:61]
	s_waitcnt vmcnt(10)
	v_mfma_f32_16x16x32_bf16 v[54:57], v[174:177], v[198:201], v[54:57]
	v_mfma_f32_16x16x32_bf16 v[50:53], v[166:169], v[194:197], v[50:53]
	v_mfma_f32_16x16x32_bf16 v[46:49], v[174:177], v[194:197], v[46:49]
	v_mfma_f32_16x16x32_bf16 v[42:45], v[166:169], v[202:205], v[42:45]
	v_mfma_f32_16x16x32_bf16 v[14:17], v[174:177], v[202:205], v[14:17]
